# v9: P13 work split - 192 workgroups route (2-3 blocks each) while 64 sweep expert-weight tiles, instead of odd/even halves
# speedup vs baseline: 1.0428x; 1.0092x over previous
; #define MKCTX() const Ctx P{InTbl{in_tbl()}, (float*)*(__attribute__((address_space(1))) float* const*)((const char*)in_tbl() + offsetof(Params, out)), ws}
; #define IN(k) (((PH_MASK >> (k)) & 1) && KARG_I(ph_lo) <= (k) && (k) < KARG_I(ph_hi))
; #define SEAM(k) do { if (IN(k) && IN((k) + 1)) { XcdBarrier bar_; bar_.bar = (unsigned*)(ws + WS_CTL) + CW_BAR; bar_.x = xb_xcc_id(); bar_.st = MISC + 8; bar_.G = (unsigned)KARG_I(grid); xcd_barrier(bar_); } } while (0)
; __global__ void __launch_bounds__(512, 2) fwd_kernel(Params KP) {
;     ...
;     if (IN(13)) { MKCTX();
;         if (vcu & 1) { phase_router(P, lds, vcu, G); __syncthreads(); tr_slack(P, lds, (unsigned*)(ws + WS_CTL) + CW_TILE, nullptr, 0u); }
;         else { tr_slack(P, lds, (unsigned*)(ws + WS_CTL) + CW_TILE, nullptr, 0u); __syncthreads(); phase_router(P, lds, vcu, G); } } SEAM(13);
.LBB0_2331:
	s_or_b64 exec, exec, s[40:41]
	s_mov_b64 s[2:3], s[0:1]
	s_nop 0
	v_mov_b64_e32 v[2:3], s[2:3]
	flat_load_dword v1, v[2:3] offset:296
	s_waitcnt vmcnt(0) lgkmcnt(0)
	v_cmp_gt_i32_e32 vcc, 14, v1
	s_and_saveexec_b64 s[26:27], vcc
	s_cbranch_execz .LBB0_2466
	s_mov_b64 s[2:3], s[0:1]
	s_nop 0
	v_mov_b64_e32 v[2:3], s[2:3]
	flat_load_dword v1, v[2:3] offset:300
	s_waitcnt vmcnt(0) lgkmcnt(0)
	v_cmp_lt_i32_e32 vcc, 13, v1
	s_and_b64 exec, exec, vcc
	s_cbranch_execz .LBB0_2466
	s_mov_b64 s[28:29], s[0:1]
	s_mov_b64 s[2:3], s[0:1]
	s_and_b32 s99, s33, 3
	s_cmp_eq_u32 s99, 0
	s_mov_b64 s[2:3], -1
	s_cbranch_scc1 .LBB0_2400
	v_mov_b64_e32 v[2:3], s[28:29]
	flat_load_dwordx2 v[2:3], v[2:3] offset:232
	v_or_b32_e32 v1, 0x200, v0
	v_mov_b32_e32 v8, 16
	s_mov_b64 s[2:3], 0
	v_mov_b32_e32 v7, 0
	v_mov_b64_e32 v[4:5], v[0:1]

; #define LAS __attribute__((address_space(3)))
; __device__ __forceinline__ void phase_router(const Ctx& P, LAS unsigned char* lds, int vcu, int G) {
;     const int tid = threadIdx.x, lane = tid & 63, wave = __builtin_amdgcn_readfirstlane(tid >> 6);
;     LAS float* rwT = (LAS float*)lds;
;     LAS unsigned char* rows8 = lds + 65536;
;     LAS int* sel = (LAS int*)(lds + LDS_MISC + 1024);
;     LAS float* prb = (LAS float*)(lds + LDS_MISC + 1024 + 256);
;     LAS int* lrank = (LAS int*)(lds + LDS_MISC + 1024 + 512);
;     LAS int* lcnt = (LAS int*)(lds + LDS_MISC + 1024 + 768);
;     LAS int* lbase = (LAS int*)(lds + LDS_MISC + 1024 + 832);
;     LAS float* rscl = (LAS float*)(lds + LDS_MISC + 1024 + 864);
;     for (int i = tid; i < DM * 8; i += 512) { const int k = i >> 3, e = i & 7; rwT[e * DM + k] = P.in[29][i]; }
;     __syncthreads();
;     const float* mod = (const float*)(P.ws + WS_MOD) + (size_t)5 * NMOD;
;     const float* gvec = P.in[7] + DM;
;     unsigned char* HNP = P.ws + WS_HNP; unsigned* ecnt = (unsigned*)(P.ws + WS_CTL) + CW_ECNT; int* tok = (int*)(P.ws + WS_TOK);
;     for (int blk = vcu; blk < ML / 32; blk += G) {
;         if (tid < 8) lcnt[tid] = 0;
;         for (int q = 0; q < 4; ++q) {
.LBB0_2342:
	s_or_b64 exec, exec, s[2:3]
	v_and_b32_e32 v1, 63, v0
	v_readfirstlane_b32 s12, v0
	s_cmpk_gt_i32 s33, 0x1ff
	v_lshlrev_b32_e32 v74, 2, v1
	s_waitcnt lgkmcnt(0)
	s_barrier
	s_cbranch_scc1 .LBB0_2377
	v_mov_b64_e32 v[2:3], s[28:29]
	flat_load_dwordx2 v[2:3], v[2:3] offset:56
	s_add_u32 s9, s36, 0x13c000
	v_mov_b32_e32 v11, 0
	v_mbcnt_lo_u32_b32 v7, -1, 0
	v_lshlrev_b32_e32 v10, 8, v0
	s_addc_u32 s38, s37, 0
	s_mov_b64 s[14:15], 0x4000
	v_mbcnt_hi_u32_b32 v7, -1, v7
	v_lshl_add_u64 v[12:13], s[36:37], 0, v[10:11]
	s_add_u32 s30, s36, 0x200000
	v_and_b32_e32 v9, 64, v7
	v_lshl_add_u64 v[12:13], v[12:13], 0, s[14:15]
	s_addc_u32 s31, s37, 0
	s_lshr_b32 s14, s12, 4
	v_xor_b32_e32 v14, 1, v7
	s_add_i32 s13, 0, 0x20700
	v_add_u32_e32 v9, 64, v9
	s_and_b32 s46, s14, 0xffffffc
	v_lshlrev_b32_e32 v5, 2, v0
	v_xor_b32_e32 v15, 2, v7
	v_cmp_lt_i32_e32 vcc, v14, v9
	s_add_u32 s47, s36, 0x1c2c0000
	v_add_u32_e32 v62, s13, v5
	v_cndmask_b32_e32 v14, v7, v14, vcc
	v_cmp_lt_i32_e32 vcc, v15, v9
	s_addc_u32 s48, s37, 0
	s_add_i32 s72, 0, 0x20600
	s_add_i32 s71, 0, 0x20400
	s_add_i32 s13, 0, 0x20740
	s_add_i32 s15, 0, 0x20500
	s_mov_b64 s[10:11], 0x2000
	v_cndmask_b32_e32 v15, v7, v15, vcc
	s_add_u32 s34, s36, 0x5cf30000
	v_lshlrev_b32_e32 v63, 2, v14
	v_lshlrev_b32_e32 v64, 2, v15
	s_addc_u32 s35, s37, 0
	s_add_i32 s76, 0, 0x10000
	s_add_i32 s68, 0, 0x20760
	v_xor_b32_e32 v16, 4, v7
	v_lshlrev_b32_e32 v10, 4, v1
	v_xor_b32_e32 v17, 8, v7
	v_cmp_lt_i32_e32 vcc, v16, v9
	v_add_u32_e32 v69, s72, v5
	v_add_u32_e32 v70, s71, v5
	v_xor_b32_e32 v25, 16, v7
	v_cndmask_b32_e32 v16, v7, v16, vcc
	v_cmp_lt_i32_e32 vcc, v17, v9
	v_lshl_add_u64 v[32:33], s[36:37], 0, v[10:11]
	v_xor_b32_e32 v26, 32, v7
	v_cndmask_b32_e32 v17, v7, v17, vcc
	v_cmp_lt_i32_e32 vcc, v25, v9
	v_or_b32_e32 v4, 0x100, v74
	v_or_b32_e32 v6, 0x200, v74
	v_or_b32_e32 v8, 0x300, v74
	v_or_b32_e32 v34, 0x400, v74
	v_cndmask_b32_e32 v25, v7, v25, vcc
	v_cmp_lt_i32_e32 vcc, v26, v9
	v_or_b32_e32 v36, 0x600, v74
	v_or_b32_e32 v38, 0x700, v74
	v_and_b32_e32 v58, 1, v0
	v_lshlrev_b32_e32 v18, 2, v4
	v_mov_b32_e32 v19, v11
	v_lshlrev_b32_e32 v20, 2, v6
	v_mov_b32_e32 v21, v11
	v_lshlrev_b32_e32 v22, 2, v8
	v_mov_b32_e32 v23, v11
	v_lshlrev_b32_e32 v24, 2, v34
	v_cndmask_b32_e32 v7, v7, v26, vcc
	v_lshlrev_b32_e32 v67, 2, v25
	v_mov_b32_e32 v25, v11
	v_mov_b32_e32 v27, v11
	v_lshlrev_b32_e32 v28, 2, v36
	v_mov_b32_e32 v29, v11
	v_lshlrev_b32_e32 v30, 2, v38
	v_mov_b32_e32 v31, v11
	v_cmp_gt_u32_e64 s[2:3], 8, v0
	v_cmp_eq_u32_e64 s[4:5], 0, v1
	v_cmp_gt_u32_e64 s[6:7], 64, v0
	v_and_b32_e32 v59, 0xf8, v5
	v_lshlrev_b32_e32 v60, 1, v58
	s_waitcnt vmcnt(0) lgkmcnt(0)
	v_lshl_add_u64 v[14:15], v[2:3], 0, s[10:11]
	s_lshl_b32 s10, s46, 11
	s_add_i32 s49, s76, s10
	s_lshl_b32 s10, s46, 2
	s_add_i32 s50, s68, s10
	s_lshl_b32 s10, s46, 3
	s_add_i32 s51, s71, s10
	s_add_i32 s52, s72, s10
	s_or_b32 s10, s10, 4
	s_add_i32 s53, s71, s10
	s_add_i32 s54, s72, s10
	s_or_b32 s10, s46, 1
	s_lshl_b32 s11, s10, 11
	s_add_i32 s55, s76, s11
	s_lshl_b32 s11, s10, 2
	s_lshl_b32 s10, s10, 3
	s_add_i32 s57, s71, s10
	s_add_i32 s58, s72, s10
	s_or_b32 s10, s10, 4
	s_add_i32 s59, s71, s10
	s_add_i32 s60, s72, s10
	s_or_b32 s10, s46, 2
	s_add_i32 s56, s68, s11
	s_lshl_b32 s11, s10, 11
	s_add_i32 s61, s76, s11
	s_lshl_b32 s11, s10, 2
	s_lshl_b32 s10, s10, 3
	s_add_i32 s63, s71, s10
	s_add_i32 s64, s72, s10
	s_or_b32 s10, s10, 4
	s_add_i32 s65, s71, s10
	s_add_i32 s66, s72, s10
	s_or_b32 s10, s14, 3
	s_add_i32 s62, s68, s11
	s_lshl_b32 s11, s10, 11
	s_add_i32 s67, s76, s11
	s_lshl_b32 s11, s10, 2
	s_lshl_b32 s10, s10, 3
	s_add_i32 s69, s71, s10
	s_add_i32 s70, s72, s10
	s_or_b32 s10, s10, 4
	s_add_i32 s68, s68, s11
	s_add_i32 s71, s71, s10
	s_add_i32 s72, s72, s10
	s_mov_b64 s[10:11], 0x4aec0000
	s_add_u32 s73, s36, 0x1c2c0200
	v_lshl_add_u64 v[32:33], v[32:33], 0, s[10:11]
	s_addc_u32 s74, s37, 0
	s_lshr_b32 s99, s33, 2
	s_mul_i32 s99, s99, 3
	s_and_b32 s10, s33, 3
	s_add_i32 s99, s99, s10
	s_add_i32 s99, s99, -1
	s_lshl_b32 s10, s99, 5
	v_or_b32_e32 v2, 0x500, v74
	s_add_i32 s40, s10, s46
	s_lshl_b32 s10, s12, 7
	v_lshlrev_b32_e32 v26, 2, v2
	s_and_b32 s10, s10, 0xffffe000
	v_add_u32_e32 v61, 0, v10
	v_lshlrev_b32_e32 v65, 2, v16
	v_lshlrev_b32_e32 v66, 2, v17
	v_lshlrev_b32_e32 v68, 2, v7
	v_add_u32_e32 v71, s13, v5
	v_add_u32_e32 v72, s15, v5
	v_lshl_add_u64 v[16:17], v[14:15], 0, v[10:11]
	v_lshl_add_u64 v[18:19], v[14:15], 0, v[18:19]
	v_lshl_add_u64 v[20:21], v[14:15], 0, v[20:21]
	v_lshl_add_u64 v[22:23], v[14:15], 0, v[22:23]
	v_lshl_add_u64 v[24:25], v[14:15], 0, v[24:25]
	v_lshl_add_u64 v[26:27], v[14:15], 0, v[26:27]
	v_lshl_add_u64 v[28:29], v[14:15], 0, v[28:29]
	v_lshl_add_u64 v[30:31], v[14:15], 0, v[30:31]
	s_movk_i32 s75, 0x1800
	s_add_i32 s76, s76, s10
	v_mov_b32_e32 v73, 0x358637bd
	v_lshlrev_b32_e32 v75, 2, v4
	v_lshlrev_b32_e32 v76, 2, v6
	v_lshlrev_b32_e32 v77, 2, v8
	v_lshlrev_b32_e32 v78, 2, v34
	v_lshlrev_b32_e32 v79, 2, v2
	v_lshlrev_b32_e32 v80, 2, v36
	v_lshlrev_b32_e32 v81, 2, v38
	s_mov_b32 s77, 0xda24260
	s_mov_b32 s78, 0x42fe0000
	s_mov_b32 s79, 0x4b3fff81
	s_mov_b32 s80, 0xc0c0400
	s_mov_b32 s81, 0x5040100
	s_mov_b32 s82, 0xff61b1e6
	v_mov_b32_e32 v82, 1
	v_mov_b32_e32 v83, 0x4b40007f
	v_mov_b32_e32 v84, 0xff61b1e6
	s_mov_b32 s83, s99
	s_branch .LBB0_2345
.LBB0_2344:
	s_or_b64 exec, exec, s[10:11]
	s_addk_i32 s83, 0xc0
	s_add_i32 s40, s40, s75
	s_cmpk_lt_i32 s83, 0x200
	s_barrier
	s_cbranch_scc0 .LBB0_2377

; #define SEAM(k) do { if (IN(k) && IN((k) + 1)) { XcdBarrier bar_; bar_.bar = (unsigned*)(ws + WS_CTL) + CW_BAR; bar_.x = xb_xcc_id(); bar_.st = MISC + 8; bar_.G = (unsigned)KARG_I(grid); xcd_barrier(bar_); } } while (0)
; __device__ __forceinline__ void phase_router(const Ctx& P, LAS unsigned char* lds, int vcu, int G) {
;     ...
;     for (int blk = vcu; blk < ML / 32; blk += G) {
; __global__ void __launch_bounds__(512, 2) fwd_kernel(Params KP) {
;     ...
;         if (vcu & 1) { phase_router(P, lds, vcu, G); __syncthreads(); tr_slack(P, lds, (unsigned*)(ws + WS_CTL) + CW_TILE, nullptr, 0u); }
;         else { tr_slack(P, lds, (unsigned*)(ws + WS_CTL) + CW_TILE, nullptr, 0u); __syncthreads(); phase_router(P, lds, vcu, G); } } SEAM(13);
.LBB0_2431:
	s_or_b64 exec, exec, s[2:3]
	v_readfirstlane_b32 s12, v0
	s_cmp_eq_u32 s33, s33
	s_waitcnt lgkmcnt(0)
	s_barrier
	s_cbranch_scc1 .LBB0_2466
	v_mov_b64_e32 v[2:3], s[28:29]
	flat_load_dwordx2 v[2:3], v[2:3] offset:56
	s_add_u32 s9, s36, 0x13c000
	v_mov_b32_e32 v11, 0
	v_mbcnt_lo_u32_b32 v7, -1, 0
	v_lshlrev_b32_e32 v10, 8, v0
	s_addc_u32 s38, s37, 0
	s_mov_b64 s[14:15], 0x4000
	v_mbcnt_hi_u32_b32 v7, -1, v7
	v_lshl_add_u64 v[12:13], s[36:37], 0, v[10:11]
	s_add_u32 s30, s36, 0x200000
	v_and_b32_e32 v9, 64, v7
	v_lshl_add_u64 v[12:13], v[12:13], 0, s[14:15]
	s_addc_u32 s31, s37, 0
	s_lshr_b32 s14, s12, 4
	v_xor_b32_e32 v14, 1, v7
	s_add_i32 s13, 0, 0x20700
	v_add_u32_e32 v9, 64, v9
	s_and_b32 s46, s14, 0xffffffc
	v_lshlrev_b32_e32 v5, 2, v0
	v_xor_b32_e32 v15, 2, v7
	v_cmp_lt_i32_e32 vcc, v14, v9
	s_add_u32 s47, s36, 0x1c2c0000
	v_add_u32_e32 v61, s13, v5
	v_cndmask_b32_e32 v14, v7, v14, vcc
	v_cmp_lt_i32_e32 vcc, v15, v9
	s_addc_u32 s48, s37, 0
	s_add_i32 s72, 0, 0x20600
	s_add_i32 s71, 0, 0x20400
	s_add_i32 s13, 0, 0x20740
	s_add_i32 s15, 0, 0x20500
	s_mov_b64 s[10:11], 0x2000
	v_cndmask_b32_e32 v15, v7, v15, vcc
	s_add_u32 s34, s36, 0x5cf30000
	v_lshlrev_b32_e32 v62, 2, v14
	v_lshlrev_b32_e32 v63, 2, v15
	s_addc_u32 s35, s37, 0
	s_add_i32 s76, 0, 0x10000
	s_add_i32 s68, 0, 0x20760
	v_xor_b32_e32 v16, 4, v7
	v_lshlrev_b32_e32 v10, 4, v75
	v_xor_b32_e32 v17, 8, v7
	v_cmp_lt_i32_e32 vcc, v16, v9
	v_add_u32_e32 v68, s72, v5
	v_add_u32_e32 v69, s71, v5
	v_xor_b32_e32 v25, 16, v7
	v_cndmask_b32_e32 v16, v7, v16, vcc
	v_cmp_lt_i32_e32 vcc, v17, v9
	v_lshl_add_u64 v[32:33], s[36:37], 0, v[10:11]
	v_xor_b32_e32 v26, 32, v7
	v_cndmask_b32_e32 v17, v7, v17, vcc
	v_cmp_lt_i32_e32 vcc, v25, v9
	v_or_b32_e32 v4, 0x100, v74
	v_or_b32_e32 v6, 0x200, v74
	v_or_b32_e32 v8, 0x300, v74
	v_or_b32_e32 v34, 0x400, v74
	v_cndmask_b32_e32 v25, v7, v25, vcc
	v_cmp_lt_i32_e32 vcc, v26, v9
	v_or_b32_e32 v36, 0x600, v74
	v_or_b32_e32 v38, 0x700, v74
	v_and_b32_e32 v1, 1, v0
	v_lshlrev_b32_e32 v18, 2, v4
	v_mov_b32_e32 v19, v11
	v_lshlrev_b32_e32 v20, 2, v6
	v_mov_b32_e32 v21, v11
	v_lshlrev_b32_e32 v22, 2, v8
	v_mov_b32_e32 v23, v11
	v_lshlrev_b32_e32 v24, 2, v34
	v_cndmask_b32_e32 v7, v7, v26, vcc
	v_lshlrev_b32_e32 v66, 2, v25
	v_mov_b32_e32 v25, v11
	v_mov_b32_e32 v27, v11
	v_lshlrev_b32_e32 v28, 2, v36
	v_mov_b32_e32 v29, v11
	v_lshlrev_b32_e32 v30, 2, v38
	v_mov_b32_e32 v31, v11
	v_cmp_gt_u32_e64 s[2:3], 8, v0
	v_cmp_eq_u32_e64 s[4:5], 0, v75
	v_cmp_gt_u32_e64 s[6:7], 64, v0
	v_and_b32_e32 v58, 0xf8, v5
	v_lshlrev_b32_e32 v59, 1, v1
	s_waitcnt vmcnt(0) lgkmcnt(0)
	v_lshl_add_u64 v[14:15], v[2:3], 0, s[10:11]
	s_lshl_b32 s10, s46, 11
	s_add_i32 s49, s76, s10
	s_lshl_b32 s10, s46, 2
	s_add_i32 s50, s68, s10
	s_lshl_b32 s10, s46, 3
	s_add_i32 s51, s71, s10
	s_add_i32 s52, s72, s10
	s_or_b32 s10, s10, 4
	s_add_i32 s53, s71, s10
	s_add_i32 s54, s72, s10
	s_or_b32 s10, s46, 1
	s_lshl_b32 s11, s10, 11
	s_add_i32 s55, s76, s11
	s_lshl_b32 s11, s10, 2
	s_lshl_b32 s10, s10, 3
	s_add_i32 s57, s71, s10
	s_add_i32 s58, s72, s10
	s_or_b32 s10, s10, 4
	s_add_i32 s59, s71, s10
	s_add_i32 s60, s72, s10
	s_or_b32 s10, s46, 2
	s_add_i32 s56, s68, s11
	s_lshl_b32 s11, s10, 11
	s_add_i32 s61, s76, s11
	s_lshl_b32 s11, s10, 2
	s_lshl_b32 s10, s10, 3
	s_add_i32 s63, s71, s10
	s_add_i32 s64, s72, s10
	s_or_b32 s10, s10, 4
	s_add_i32 s65, s71, s10
	s_add_i32 s66, s72, s10
	s_or_b32 s10, s14, 3
	s_add_i32 s62, s68, s11
	s_lshl_b32 s11, s10, 11
	s_add_i32 s67, s76, s11
	s_lshl_b32 s11, s10, 2
	s_lshl_b32 s10, s10, 3
	s_add_i32 s69, s71, s10
	s_add_i32 s70, s72, s10
	s_or_b32 s10, s10, 4
	s_add_i32 s68, s68, s11
	s_add_i32 s71, s71, s10
	s_add_i32 s72, s72, s10
	s_mov_b64 s[10:11], 0x4aec0000
	s_add_u32 s73, s36, 0x1c2c0200
	v_lshl_add_u64 v[32:33], v[32:33], 0, s[10:11]
	s_addc_u32 s74, s37, 0
	s_lshl_b32 s10, s33, 5
	v_or_b32_e32 v2, 0x500, v74
	s_add_i32 s40, s10, s46
	s_lshl_b32 s10, s12, 7
	v_lshlrev_b32_e32 v26, 2, v2
	s_and_b32 s10, s10, 0xffffe000
	v_add_u32_e32 v60, 0, v10
	v_lshlrev_b32_e32 v64, 2, v16
	v_lshlrev_b32_e32 v65, 2, v17
	v_lshlrev_b32_e32 v67, 2, v7
	v_add_u32_e32 v70, s13, v5
	v_add_u32_e32 v71, s15, v5
	v_lshl_add_u64 v[16:17], v[14:15], 0, v[10:11]
	v_lshl_add_u64 v[18:19], v[14:15], 0, v[18:19]
	v_lshl_add_u64 v[20:21], v[14:15], 0, v[20:21]
	v_lshl_add_u64 v[22:23], v[14:15], 0, v[22:23]
	v_lshl_add_u64 v[24:25], v[14:15], 0, v[24:25]
	v_lshl_add_u64 v[26:27], v[14:15], 0, v[26:27]
	v_lshl_add_u64 v[28:29], v[14:15], 0, v[28:29]
	v_lshl_add_u64 v[30:31], v[14:15], 0, v[30:31]
	s_lshl_b32 s75, s39, 5
	s_add_i32 s76, s76, s10
	v_mov_b32_e32 v72, 0x358637bd
	v_lshlrev_b32_e32 v73, 2, v4
	v_lshlrev_b32_e32 v76, 2, v6
	v_lshlrev_b32_e32 v77, 2, v8
	v_lshlrev_b32_e32 v78, 2, v34
	v_lshlrev_b32_e32 v79, 2, v2
	v_lshlrev_b32_e32 v80, 2, v36
	v_lshlrev_b32_e32 v81, 2, v38
	s_mov_b32 s77, 0xda24260
	s_mov_b32 s78, 0x42fe0000
	s_mov_b32 s79, 0x4b3fff81
	s_mov_b32 s80, 0xc0c0400
	s_mov_b32 s81, 0x5040100
	s_mov_b32 s82, 0xff61b1e6
	v_mov_b32_e32 v82, 1
	v_mov_b32_e32 v83, 0x4b40007f
	v_mov_b32_e32 v84, 0xff61b1e6
	s_mov_b32 s83, s33
	s_branch .LBB0_2434
